# k12 plus write-through (sc0 sc1) stores in the per-layer-embedding GEMM epilogue
# baseline (speedup 1.0000x reference)
.LBB0_1445:
	s_add_u32 s40, s30, 0xfff80080
	s_addc_u32 s41, s31, -1
	s_add_i32 s72, 0, 0x10000
	v_add_u32_e32 v60, s72, v244
	ds_read_b128 v[36:39], v60
	ds_read_b128 v[44:47], v60 offset:1024
	ds_read_b128 v[52:55], v60 offset:2048
	ds_read_b128 v[60:63], v60 offset:3072
	s_cmp_eq_u32 s28, 28
	s_cselect_b32 s43, s15, s41
	s_cselect_b32 s42, s19, s40
	s_cselect_b32 s41, vcc_lo, s65
	s_cselect_b32 s40, vcc_hi, s64
	v_lshl_add_u64 v[172:173], s[30:31], 0, v[222:223]
	s_add_i32 m0, s27, 0xc000
	ds_read_b128 v[120:123], v247
	ds_read_b128 v[124:127], v247 offset:1024
	ds_read_b128 v[132:135], v247 offset:2048
	ds_read_b128 v[136:139], v247 offset:3072
	ds_read_b128 v[148:151], v247 offset:4096
	ds_read_b128 v[152:155], v247 offset:5120
	ds_read_b128 v[164:167], v247 offset:6144
	ds_read_b128 v[168:171], v247 offset:7168
	global_load_lds_dwordx4 v[172:173], off
	v_lshl_add_u64 v[172:173], s[30:31], 0, v[224:225]
	s_add_i32 m0, s27, 0xe000
	s_nop 0
	global_load_lds_dwordx4 v[172:173], off
	s_waitcnt lgkmcnt(8)
	s_barrier
	s_waitcnt lgkmcnt(0)
	s_setprio 1
	s_waitcnt lgkmcnt(0)
	v_mfma_f32_16x16x32_bf16 v[160:163], v[52:55], v[120:123], v[160:163]
	v_mfma_f32_16x16x32_bf16 v[140:143], v[36:39], v[132:135], v[140:143]
	v_mfma_f32_16x16x32_bf16 v[128:131], v[52:55], v[132:135], v[128:131]
	v_mfma_f32_16x16x32_bf16 v[108:111], v[36:39], v[148:151], v[108:111]
	v_mfma_f32_16x16x32_bf16 v[104:107], v[52:55], v[148:151], v[104:107]
	v_mfma_f32_16x16x32_bf16 v[92:95], v[36:39], v[164:167], v[92:95]
	v_mfma_f32_16x16x32_bf16 v[88:91], v[52:55], v[164:167], v[88:91]
	v_mfma_f32_16x16x32_bf16 v[172:175], v[36:39], v[120:123], v[180:183]
	v_mfma_f32_16x16x32_bf16 v[160:163], v[60:63], v[124:127], v[160:163]
	v_mfma_f32_16x16x32_bf16 v[140:143], v[44:47], v[136:139], v[140:143]
	v_mfma_f32_16x16x32_bf16 v[128:131], v[60:63], v[136:139], v[128:131]
	v_mfma_f32_16x16x32_bf16 v[108:111], v[44:47], v[152:155], v[108:111]
	v_mfma_f32_16x16x32_bf16 v[104:107], v[60:63], v[152:155], v[104:107]
	v_mfma_f32_16x16x32_bf16 v[92:95], v[44:47], v[168:171], v[92:95]
	v_mfma_f32_16x16x32_bf16 v[88:91], v[60:63], v[168:171], v[88:91]
	v_mfma_f32_16x16x32_bf16 v[172:175], v[44:47], v[124:127], v[172:175]
	s_setprio 0
	s_barrier
	s_add_i32 s77, 0, 0x14000
	s_add_i32 s72, s72, s62
	v_add_u32_e32 v188, s77, v244
	v_lshl_add_u64 v[196:197], s[40:41], 0, v[208:209]
	s_mov_b32 m0, s72
	ds_read_b128 v[176:179], v188
	ds_read_b128 v[180:183], v188 offset:1024
	ds_read_b128 v[184:187], v188 offset:2048
	ds_read_b128 v[188:191], v188 offset:3072
	global_load_lds_dwordx4 v[196:197], off
	v_lshl_add_u64 v[198:199], s[40:41], 0, v[220:221]
	s_add_i32 m0, s72, 0x2000
	s_nop 0
	global_load_lds_dwordx4 v[198:199], off
	s_barrier
	s_waitcnt lgkmcnt(0)
	s_setprio 1
	s_waitcnt lgkmcnt(0)
	v_mfma_f32_16x16x32_bf16 v[156:159], v[176:179], v[120:123], v[156:159]
	v_mfma_f32_16x16x32_bf16 v[116:119], v[176:179], v[132:135], v[116:119]
	v_mfma_f32_16x16x32_bf16 v[112:115], v[184:187], v[132:135], v[112:115]
	v_mfma_f32_16x16x32_bf16 v[100:103], v[176:179], v[148:151], v[100:103]
	v_mfma_f32_16x16x32_bf16 v[96:99], v[184:187], v[148:151], v[96:99]
	v_mfma_f32_16x16x32_bf16 v[84:87], v[176:179], v[164:167], v[84:87]
	v_mfma_f32_16x16x32_bf16 v[80:83], v[184:187], v[164:167], v[80:83]
	v_mfma_f32_16x16x32_bf16 v[156:159], v[180:183], v[124:127], v[156:159]
	v_mfma_f32_16x16x32_bf16 v[120:123], v[184:187], v[120:123], v[144:147]
	v_mfma_f32_16x16x32_bf16 v[116:119], v[180:183], v[136:139], v[116:119]
	v_mfma_f32_16x16x32_bf16 v[112:115], v[188:191], v[136:139], v[112:115]
	v_mfma_f32_16x16x32_bf16 v[100:103], v[180:183], v[152:155], v[100:103]
	v_mfma_f32_16x16x32_bf16 v[96:99], v[188:191], v[152:155], v[96:99]
	v_mfma_f32_16x16x32_bf16 v[84:87], v[180:183], v[168:171], v[84:87]
	v_mfma_f32_16x16x32_bf16 v[80:83], v[188:191], v[168:171], v[80:83]
	v_mfma_f32_16x16x32_bf16 v[120:123], v[188:191], v[124:127], v[120:123]
	s_setprio 0
	s_mov_b32 m0, s27
	v_lshl_add_u64 v[200:201], s[42:43], 0, v[208:209]
	s_barrier
	ds_read_b128 v[124:127], v247 offset:16384
	ds_read_b128 v[132:135], v247 offset:17408
	ds_read_b128 v[136:139], v247 offset:18432
	ds_read_b128 v[144:147], v247 offset:19456
	ds_read_b128 v[148:151], v247 offset:20480
	ds_read_b128 v[152:155], v247 offset:21504
	ds_read_b128 v[164:167], v247 offset:22528
	ds_read_b128 v[168:171], v247 offset:23552
	global_load_lds_dwordx4 v[200:201], off
	v_lshl_add_u64 v[202:203], s[42:43], 0, v[220:221]
	s_mov_b32 m0, s63
	s_nop 0
	global_load_lds_dwordx4 v[202:203], off
	s_barrier
	s_waitcnt lgkmcnt(0)
	s_setprio 1
	s_waitcnt lgkmcnt(0)
	v_mfma_f32_16x16x32_bf16 v[76:79], v[36:39], v[124:127], v[76:79]
	v_mfma_f32_16x16x32_bf16 v[72:75], v[52:55], v[124:127], v[72:75]
	v_mfma_f32_16x16x32_bf16 v[56:59], v[36:39], v[136:139], v[56:59]
	v_mfma_f32_16x16x32_bf16 v[48:51], v[52:55], v[136:139], v[48:51]
	v_mfma_f32_16x16x32_bf16 v[28:31], v[36:39], v[148:151], v[28:31]
	v_mfma_f32_16x16x32_bf16 v[24:27], v[52:55], v[148:151], v[24:27]
	v_mfma_f32_16x16x32_bf16 v[12:15], v[36:39], v[164:167], v[12:15]
	v_mfma_f32_16x16x32_bf16 v[8:11], v[52:55], v[164:167], v[8:11]
	v_mfma_f32_16x16x32_bf16 v[76:79], v[44:47], v[132:135], v[76:79]
	v_mfma_f32_16x16x32_bf16 v[72:75], v[60:63], v[132:135], v[72:75]
	v_mfma_f32_16x16x32_bf16 v[56:59], v[44:47], v[144:147], v[56:59]
	v_mfma_f32_16x16x32_bf16 v[48:51], v[60:63], v[144:147], v[48:51]
	v_mfma_f32_16x16x32_bf16 v[28:31], v[44:47], v[152:155], v[28:31]
	v_mfma_f32_16x16x32_bf16 v[24:27], v[60:63], v[152:155], v[24:27]
	v_mfma_f32_16x16x32_bf16 v[12:15], v[44:47], v[168:171], v[12:15]
	v_mfma_f32_16x16x32_bf16 v[8:11], v[60:63], v[168:171], v[8:11]
	s_setprio 0
	s_barrier
	s_add_u32 s72, s40, 0x80000
	s_addc_u32 s73, s41, 0
	s_add_i32 s77, s77, s62
	v_lshl_add_u64 v[36:37], s[72:73], 0, v[208:209]
	s_mov_b32 m0, s77
	s_nop 0
	global_load_lds_dwordx4 v[36:37], off
	v_lshl_add_u64 v[36:37], s[72:73], 0, v[220:221]
	s_add_i32 m0, s77, 0x2000
	s_nop 0
	global_load_lds_dwordx4 v[36:37], off
	s_waitcnt vmcnt(6)
	s_barrier
	s_setprio 1
	v_mfma_f32_16x16x32_bf16 v[40:43], v[176:179], v[136:139], v[40:43]
	v_mfma_f32_16x16x32_bf16 v[32:35], v[184:187], v[136:139], v[32:35]
	v_mfma_f32_16x16x32_bf16 v[20:23], v[176:179], v[148:151], v[20:23]
	v_mfma_f32_16x16x32_bf16 v[16:19], v[184:187], v[148:151], v[16:19]
	v_mfma_f32_16x16x32_bf16 v[4:7], v[176:179], v[164:167], v[4:7]
	v_mfma_f32_16x16x32_bf16 v[0:3], v[184:187], v[164:167], v[0:3]
	v_mfma_f32_16x16x32_bf16 v[36:39], v[176:179], v[124:127], v[68:71]
	v_mfma_f32_16x16x32_bf16 v[44:47], v[184:187], v[124:127], v[64:67]
	v_mfma_f32_16x16x32_bf16 v[40:43], v[180:183], v[144:147], v[40:43]
	v_mfma_f32_16x16x32_bf16 v[32:35], v[188:191], v[144:147], v[32:35]
	v_mfma_f32_16x16x32_bf16 v[20:23], v[180:183], v[152:155], v[20:23]
	v_mfma_f32_16x16x32_bf16 v[16:19], v[188:191], v[152:155], v[16:19]
	v_mfma_f32_16x16x32_bf16 v[4:7], v[180:183], v[168:171], v[4:7]
	v_mfma_f32_16x16x32_bf16 v[0:3], v[188:191], v[168:171], v[0:3]
	v_mfma_f32_16x16x32_bf16 v[36:39], v[180:183], v[132:135], v[36:39]
	v_mfma_f32_16x16x32_bf16 v[44:47], v[188:191], v[132:135], v[44:47]
	s_setprio 0
	s_add_i32 s72, 0, 0x18000
	v_add_u32_e32 v68, s72, v244
	s_barrier
	ds_read_b128 v[52:55], v68
	ds_read_b128 v[60:63], v68 offset:1024
	ds_read_b128 v[64:67], v68 offset:2048
	ds_read_b128 v[68:71], v68 offset:3072
	s_add_u32 s42, s42, 0x80000
	s_addc_u32 s43, s43, 0
	s_mov_b32 m0, s74
	v_lshl_add_u64 v[144:145], s[42:43], 0, v[208:209]
	ds_read_b128 v[124:127], v247 offset:32768
	ds_read_b128 v[132:135], v247 offset:33792
	ds_read_b128 v[136:139], v247 offset:34816
	ds_read_b128 v[148:151], v247 offset:35840
	ds_read_b128 v[152:155], v247 offset:36864
	ds_read_b128 v[164:167], v247 offset:37888
	ds_read_b128 v[168:171], v247 offset:38912
	ds_read_b128 v[176:179], v247 offset:39936
	global_load_lds_dwordx4 v[144:145], off
	v_lshl_add_u64 v[144:145], s[42:43], 0, v[220:221]
	s_mov_b32 m0, s75
	s_nop 0
	global_load_lds_dwordx4 v[144:145], off
	s_waitcnt lgkmcnt(8)
	s_barrier
	s_waitcnt lgkmcnt(0)
	s_setprio 1
	s_waitcnt lgkmcnt(0)
	v_mfma_f32_16x16x32_bf16 v[144:147], v[52:55], v[124:127], v[172:175]
	v_mfma_f32_16x16x32_bf16 v[180:183], v[60:63], v[132:135], v[144:147]
	v_mfma_f32_16x16x32_bf16 v[144:147], v[64:67], v[124:127], v[160:163]
	v_mfma_f32_16x16x32_bf16 v[140:143], v[52:55], v[136:139], v[140:143]
	v_mfma_f32_16x16x32_bf16 v[128:131], v[64:67], v[136:139], v[128:131]
	v_mfma_f32_16x16x32_bf16 v[108:111], v[52:55], v[152:155], v[108:111]
	v_mfma_f32_16x16x32_bf16 v[104:107], v[64:67], v[152:155], v[104:107]
	v_mfma_f32_16x16x32_bf16 v[92:95], v[52:55], v[168:171], v[92:95]
	v_mfma_f32_16x16x32_bf16 v[88:91], v[64:67], v[168:171], v[88:91]
	v_mfma_f32_16x16x32_bf16 v[160:163], v[68:71], v[132:135], v[144:147]
	v_mfma_f32_16x16x32_bf16 v[140:143], v[60:63], v[148:151], v[140:143]
	v_mfma_f32_16x16x32_bf16 v[128:131], v[68:71], v[148:151], v[128:131]
	v_mfma_f32_16x16x32_bf16 v[108:111], v[60:63], v[164:167], v[108:111]
	v_mfma_f32_16x16x32_bf16 v[104:107], v[68:71], v[164:167], v[104:107]
	v_mfma_f32_16x16x32_bf16 v[92:95], v[60:63], v[176:179], v[92:95]
	v_mfma_f32_16x16x32_bf16 v[88:91], v[68:71], v[176:179], v[88:91]
	s_setprio 0
	s_barrier
	s_add_i32 s42, 0, 0x1c000
	v_add_u32_e32 v144, s42, v244
	s_add_i32 s43, s72, s62
	ds_read_b128 v[172:175], v144
	ds_read_b128 v[184:187], v144 offset:1024
	ds_read_b128 v[188:191], v144 offset:2048
	ds_read_b128 v[192:195], v144 offset:3072
	v_lshl_add_u64 v[144:145], v[196:197], 0, s[68:69]
	s_mov_b32 m0, s43
	s_nop 0
	global_load_lds_dwordx4 v[144:145], off
	v_lshl_add_u64 v[144:145], v[198:199], 0, s[68:69]
	s_add_i32 m0, s43, 0x2000
	s_nop 0
	global_load_lds_dwordx4 v[144:145], off
	s_barrier
	s_waitcnt lgkmcnt(0)
	s_setprio 1
	s_waitcnt lgkmcnt(0)
	v_mfma_f32_16x16x32_bf16 v[144:147], v[172:175], v[124:127], v[156:159]
	v_mfma_f32_16x16x32_bf16 v[120:123], v[188:191], v[124:127], v[120:123]
	v_mfma_f32_16x16x32_bf16 v[116:119], v[172:175], v[136:139], v[116:119]
	v_mfma_f32_16x16x32_bf16 v[112:115], v[188:191], v[136:139], v[112:115]
	v_mfma_f32_16x16x32_bf16 v[100:103], v[172:175], v[152:155], v[100:103]
	v_mfma_f32_16x16x32_bf16 v[96:99], v[188:191], v[152:155], v[96:99]
	v_mfma_f32_16x16x32_bf16 v[84:87], v[172:175], v[168:171], v[84:87]
	v_mfma_f32_16x16x32_bf16 v[80:83], v[188:191], v[168:171], v[80:83]
	v_mfma_f32_16x16x32_bf16 v[156:159], v[184:187], v[132:135], v[144:147]
	v_mfma_f32_16x16x32_bf16 v[144:147], v[192:195], v[132:135], v[120:123]
	v_mfma_f32_16x16x32_bf16 v[116:119], v[184:187], v[148:151], v[116:119]
	v_mfma_f32_16x16x32_bf16 v[112:115], v[192:195], v[148:151], v[112:115]
	v_mfma_f32_16x16x32_bf16 v[100:103], v[184:187], v[164:167], v[100:103]
	v_mfma_f32_16x16x32_bf16 v[96:99], v[192:195], v[164:167], v[96:99]
	v_mfma_f32_16x16x32_bf16 v[84:87], v[184:187], v[176:179], v[84:87]
	v_mfma_f32_16x16x32_bf16 v[80:83], v[192:195], v[176:179], v[80:83]
	s_setprio 0
	s_mov_b32 m0, s79
	v_lshl_add_u64 v[176:177], v[200:201], 0, s[68:69]
	s_barrier
	ds_read_b128 v[120:123], v247 offset:49152
	ds_read_b128 v[124:127], v247 offset:50176
	ds_read_b128 v[132:135], v247 offset:51200
	ds_read_b128 v[136:139], v247 offset:52224
	ds_read_b128 v[148:151], v247 offset:53248
	ds_read_b128 v[152:155], v247 offset:54272
	ds_read_b128 v[164:167], v247 offset:55296
	ds_read_b128 v[168:171], v247 offset:56320
	global_load_lds_dwordx4 v[176:177], off
	v_lshl_add_u64 v[176:177], v[202:203], 0, s[68:69]
	s_mov_b32 m0, s90
	s_nop 0
	global_load_lds_dwordx4 v[176:177], off
	s_barrier
	s_waitcnt lgkmcnt(0)
	s_setprio 1
	s_waitcnt lgkmcnt(0)
	v_mfma_f32_16x16x32_bf16 v[76:79], v[52:55], v[120:123], v[76:79]
	v_mfma_f32_16x16x32_bf16 v[72:75], v[64:67], v[120:123], v[72:75]
	v_mfma_f32_16x16x32_bf16 v[56:59], v[52:55], v[132:135], v[56:59]
	v_mfma_f32_16x16x32_bf16 v[48:51], v[64:67], v[132:135], v[48:51]
	v_mfma_f32_16x16x32_bf16 v[28:31], v[52:55], v[148:151], v[28:31]
	v_mfma_f32_16x16x32_bf16 v[24:27], v[64:67], v[148:151], v[24:27]
	v_mfma_f32_16x16x32_bf16 v[12:15], v[52:55], v[164:167], v[12:15]
	v_mfma_f32_16x16x32_bf16 v[8:11], v[64:67], v[164:167], v[8:11]
	v_mfma_f32_16x16x32_bf16 v[76:79], v[60:63], v[124:127], v[76:79]
	v_mfma_f32_16x16x32_bf16 v[72:75], v[68:71], v[124:127], v[72:75]
	v_mfma_f32_16x16x32_bf16 v[56:59], v[60:63], v[136:139], v[56:59]
	v_mfma_f32_16x16x32_bf16 v[48:51], v[68:71], v[136:139], v[48:51]
	v_mfma_f32_16x16x32_bf16 v[28:31], v[60:63], v[152:155], v[28:31]
	v_mfma_f32_16x16x32_bf16 v[24:27], v[68:71], v[152:155], v[24:27]
	v_mfma_f32_16x16x32_bf16 v[12:15], v[60:63], v[168:171], v[12:15]
	v_mfma_f32_16x16x32_bf16 v[8:11], v[68:71], v[168:171], v[8:11]
	s_setprio 0
	s_barrier
	s_add_u32 s40, s40, 0x80080
	s_addc_u32 s41, s41, 0
	s_add_i32 s42, s42, s62
	v_lshl_add_u64 v[52:53], s[40:41], 0, v[208:209]
	s_mov_b32 m0, s42
	s_nop 0
	global_load_lds_dwordx4 v[52:53], off
	v_lshl_add_u64 v[52:53], s[40:41], 0, v[220:221]
	s_add_i32 m0, s42, 0x2000
	s_nop 0
	global_load_lds_dwordx4 v[52:53], off
	s_waitcnt vmcnt(6)
	s_barrier
	s_setprio 1
	v_mfma_f32_16x16x32_bf16 v[36:39], v[172:175], v[120:123], v[36:39]
	v_mfma_f32_16x16x32_bf16 v[68:71], v[184:187], v[124:127], v[36:39]
	v_mfma_f32_16x16x32_bf16 v[36:39], v[188:191], v[120:123], v[44:47]
	v_mfma_f32_16x16x32_bf16 v[64:67], v[192:195], v[124:127], v[36:39]
	v_mfma_f32_16x16x32_bf16 v[36:39], v[172:175], v[132:135], v[40:43]
	v_mfma_f32_16x16x32_bf16 v[32:35], v[188:191], v[132:135], v[32:35]
	v_mfma_f32_16x16x32_bf16 v[20:23], v[172:175], v[148:151], v[20:23]
	v_mfma_f32_16x16x32_bf16 v[16:19], v[188:191], v[148:151], v[16:19]
	v_mfma_f32_16x16x32_bf16 v[4:7], v[172:175], v[164:167], v[4:7]
	v_mfma_f32_16x16x32_bf16 v[0:3], v[188:191], v[164:167], v[0:3]
	v_mfma_f32_16x16x32_bf16 v[40:43], v[184:187], v[136:139], v[36:39]
	v_mfma_f32_16x16x32_bf16 v[32:35], v[192:195], v[136:139], v[32:35]
	v_mfma_f32_16x16x32_bf16 v[20:23], v[184:187], v[152:155], v[20:23]
	v_mfma_f32_16x16x32_bf16 v[16:19], v[192:195], v[152:155], v[16:19]
	v_mfma_f32_16x16x32_bf16 v[4:7], v[184:187], v[168:171], v[4:7]
	v_mfma_f32_16x16x32_bf16 v[0:3], v[192:195], v[168:171], v[0:3]
	s_setprio 0
	s_add_i32 s28, s28, 2
	s_add_u32 s30, s30, 0x100
	s_addc_u32 s31, s31, 0
	s_add_u32 s64, s64, 0x100
	s_addc_u32 s65, s65, 0
	s_cmp_gt_u32 s28, 29
	s_barrier
	s_cbranch_scc0 .LBB0_1445
	s_lshl_b32 s15, s26, 8
	v_lshl_or_b32 v226, s85, 8, v246
	s_add_i32 s15, s15, s78
	v_ashrrev_i32_e32 v227, 31, v226
	v_or_b32_e32 v120, s15, v243
	v_lshl_add_u64 v[44:45], v[226:227], 2, s[10:11]
	v_ashrrev_i32_e32 v121, 31, v120
	global_load_dwordx4 v[52:55], v[44:45], off offset:16
	global_load_dwordx4 v[60:63], v[44:45], off
	global_load_dwordx4 v[36:39], v[44:45], off offset:528
	s_nop 0
	global_load_dwordx4 v[44:47], v[44:45], off offset:512
	v_lshlrev_b64 v[122:123], 11, v[120:121]
	v_lshl_add_u64 v[120:121], v[120:121], 2, s[12:13]
	global_load_dword v251, v[120:121], off
	global_load_dword v250, v[120:121], off offset:64
	global_load_dword v249, v[120:121], off offset:128
	global_load_dword v248, v[120:121], off offset:192
	v_lshl_add_u64 v[120:121], v[122:123], 0, v[226:227]
	v_lshlrev_b64 v[228:229], 1, v[120:121]
	v_lshl_add_u64 v[120:121], s[4:5], 0, v[228:229]
	global_load_dwordx4 v[204:207], v[120:121], off
	v_lshl_add_u64 v[122:123], s[8:9], 0, v[228:229]
	global_load_dwordx4 v[200:203], v[122:123], off
	global_load_dwordx4 v[196:199], v[120:121], off offset:256
	global_load_dwordx4 v[192:195], v[122:123], off offset:256
	v_add_co_u32_e32 v124, vcc, s1, v120
	s_mov_b32 s85, s14
	s_nop 0
	v_addc_co_u32_e32 v125, vcc, 0, v121, vcc
	global_load_dwordx4 v[184:187], v[124:125], off
	v_add_co_u32_e32 v126, vcc, s1, v122
	s_mov_b32 s26, s18
	s_nop 0
	v_addc_co_u32_e32 v127, vcc, 0, v123, vcc
	global_load_dwordx4 v[188:191], v[126:127], off
	global_load_dwordx4 v[176:179], v[124:125], off offset:256
	global_load_dwordx4 v[172:175], v[126:127], off offset:256
	v_add_co_u32_e32 v124, vcc, s52, v120
	s_mov_b64 s[40:41], s[24:25]
	s_nop 0
	v_addc_co_u32_e32 v125, vcc, 0, v121, vcc
	global_load_dwordx4 v[164:167], v[124:125], off
	v_add_co_u32_e32 v126, vcc, s52, v122
	s_mov_b64 s[30:31], s[22:23]
	s_nop 0
	v_addc_co_u32_e32 v127, vcc, 0, v123, vcc
	global_load_dwordx4 v[168:171], v[126:127], off
	global_load_dwordx4 v[152:155], v[124:125], off offset:256
	global_load_dwordx4 v[148:151], v[126:127], off offset:256
	v_add_co_u32_e32 v120, vcc, s53, v120
	s_brev_b32 s77, 18
	s_nop 0
	v_addc_co_u32_e32 v121, vcc, 0, v121, vcc
	global_load_dwordx4 v[132:135], v[120:121], off
	v_add_co_u32_e32 v124, vcc, s53, v122
	s_waitcnt vmcnt(0)
	v_fma_f32 v180, v180, v251, v60
	v_addc_co_u32_e32 v125, vcc, 0, v123, vcc
	global_load_dwordx4 v[136:139], v[124:125], off
	s_nop 0
	global_load_dwordx4 v[120:123], v[120:121], off offset:256
	s_nop 0
	global_load_dwordx4 v[124:127], v[124:125], off offset:256
	v_fma_f32 v181, v181, v251, v61
	v_fma_f32 v182, v182, v251, v62
	v_fma_f32 v183, v183, v251, v63
	v_mul_f32_e32 v180, 0xbfb8aa3b, v180
	v_mul_f32_e32 v181, 0xbfb8aa3b, v181
	v_mul_f32_e32 v182, 0xbfb8aa3b, v182
	v_mul_f32_e32 v183, 0xbfb8aa3b, v183
	v_exp_f32_e32 v180, v180
	v_exp_f32_e32 v181, v181
	v_exp_f32_e32 v182, v182
	v_exp_f32_e32 v183, v183
	v_fma_f32 v160, v160, v251, v52
	v_fma_f32 v161, v161, v251, v53
	v_mul_f32_e32 v160, 0xbfb8aa3b, v160
	v_mul_f32_e32 v161, 0xbfb8aa3b, v161
	v_fma_f32 v162, v162, v251, v54
	v_fma_f32 v163, v163, v251, v55
	v_exp_f32_e32 v160, v160
	v_exp_f32_e32 v161, v161
	v_mul_f32_e32 v162, 0xbfb8aa3b, v162
	v_mul_f32_e32 v163, 0xbfb8aa3b, v163
	v_exp_f32_e32 v162, v162
	v_exp_f32_e32 v163, v163
	v_add_f32_e32 v180, 1.0, v180
	v_add_f32_e32 v181, 1.0, v181
	v_add_f32_e32 v182, 1.0, v182
	v_add_f32_e32 v183, 1.0, v183
	v_fma_f32 v156, v156, v251, v44
	v_fma_f32 v157, v157, v251, v45
	v_rcp_f32_e32 v180, v180
	v_rcp_f32_e32 v181, v181
	v_rcp_f32_e32 v182, v182
	v_rcp_f32_e32 v183, v183
	v_mul_f32_e32 v156, 0xbfb8aa3b, v156
	v_mul_f32_e32 v157, 0xbfb8aa3b, v157
	v_fma_f32 v158, v158, v251, v46
	v_fma_f32 v159, v159, v251, v47
	v_add_f32_e32 v160, 1.0, v160
	v_add_f32_e32 v161, 1.0, v161
	v_exp_f32_e32 v156, v156
	v_exp_f32_e32 v157, v157
	v_mul_f32_e32 v158, 0xbfb8aa3b, v158
	v_mul_f32_e32 v159, 0xbfb8aa3b, v159
	v_rcp_f32_e32 v160, v160
	v_rcp_f32_e32 v161, v161
	v_add_f32_e32 v162, 1.0, v162
	v_add_f32_e32 v163, 1.0, v163
	v_exp_f32_e32 v158, v158
	v_exp_f32_e32 v159, v159
	v_fma_f32 v144, v144, v251, v36
	v_fma_f32 v145, v145, v251, v37
	v_lshlrev_b32_e32 v212, 16, v204
	v_and_b32_e32 v213, 0xffff0000, v204
	v_lshlrev_b32_e32 v214, 16, v200
	v_and_b32_e32 v215, 0xffff0000, v200
	v_lshlrev_b32_e32 v204, 16, v205
	v_and_b32_e32 v205, 0xffff0000, v205
	v_lshlrev_b32_e32 v200, 16, v201
	v_and_b32_e32 v201, 0xffff0000, v201
	v_rcp_f32_e32 v162, v162
	v_rcp_f32_e32 v163, v163
	v_mul_f32_e32 v144, 0xbfb8aa3b, v144
	v_mul_f32_e32 v145, 0xbfb8aa3b, v145
	v_fma_f32 v146, v146, v251, v38
	v_fma_f32 v147, v147, v251, v39
	v_pk_fma_f32 v[180:181], v[180:181], v[214:215], v[212:213]
	v_pk_fma_f32 v[182:183], v[182:183], v[200:201], v[204:205]
	v_exp_f32_e32 v144, v144
	v_exp_f32_e32 v145, v145
	v_mul_f32_e32 v146, 0xbfb8aa3b, v146
	v_mul_f32_e32 v147, 0xbfb8aa3b, v147
	v_cvt_pk_bf16_f32 v180, v180, v181
	v_cvt_pk_bf16_f32 v181, v182, v183
	v_lshlrev_b32_e32 v182, 16, v206
	v_and_b32_e32 v183, 0xffff0000, v206
	v_lshlrev_b32_e32 v200, 16, v202
	v_and_b32_e32 v201, 0xffff0000, v202
	v_add_f32_e32 v156, 1.0, v156
	v_add_f32_e32 v157, 1.0, v157
	v_exp_f32_e32 v146, v146
	v_exp_f32_e32 v147, v147
	v_fma_f32 v140, v140, v250, v60
	v_fma_f32 v141, v141, v250, v61
	v_pk_fma_f32 v[160:161], v[160:161], v[200:201], v[182:183]
	v_lshlrev_b32_e32 v182, 16, v207
	v_and_b32_e32 v183, 0xffff0000, v207
	v_lshlrev_b32_e32 v200, 16, v203
	v_and_b32_e32 v201, 0xffff0000, v203
	v_rcp_f32_e32 v156, v156
	v_rcp_f32_e32 v157, v157
	v_add_f32_e32 v158, 1.0, v158
	v_add_f32_e32 v159, 1.0, v159
	v_mul_f32_e32 v140, 0xbfb8aa3b, v140
	v_mul_f32_e32 v141, 0xbfb8aa3b, v141
	v_fma_f32 v142, v142, v250, v62
	v_fma_f32 v143, v143, v250, v63
	v_pk_fma_f32 v[162:163], v[162:163], v[200:201], v[182:183]
	v_rcp_f32_e32 v158, v158
	v_rcp_f32_e32 v159, v159
	v_exp_f32_e32 v140, v140
	v_exp_f32_e32 v141, v141
	v_mul_f32_e32 v142, 0xbfb8aa3b, v142
	v_mul_f32_e32 v143, 0xbfb8aa3b, v143
	v_cvt_pk_bf16_f32 v182, v160, v161
	v_cvt_pk_bf16_f32 v183, v162, v163
	v_lshl_add_u64 v[160:161], s[6:7], 0, v[228:229]
	v_add_f32_e32 v144, 1.0, v144
	v_add_f32_e32 v145, 1.0, v145
	v_exp_f32_e32 v142, v142
	v_exp_f32_e32 v143, v143
	v_fma_f32 v128, v128, v250, v52
	v_fma_f32 v129, v129, v250, v53
	global_store_dwordx4 v[160:161], v[180:183], off sc0 sc1
	v_lshlrev_b32_e32 v162, 16, v196
	v_and_b32_e32 v163, 0xffff0000, v196
	v_lshlrev_b32_e32 v180, 16, v192
	v_and_b32_e32 v181, 0xffff0000, v192
	v_rcp_f32_e32 v144, v144
	v_rcp_f32_e32 v145, v145
	v_add_f32_e32 v146, 1.0, v146
	v_add_f32_e32 v147, 1.0, v147
	v_mul_f32_e32 v128, 0xbfb8aa3b, v128
	v_mul_f32_e32 v129, 0xbfb8aa3b, v129
	v_fma_f32 v130, v130, v250, v54
	v_fma_f32 v131, v131, v250, v55
	v_pk_fma_f32 v[156:157], v[156:157], v[180:181], v[162:163]
	v_lshlrev_b32_e32 v162, 16, v197
	v_and_b32_e32 v163, 0xffff0000, v197
	v_lshlrev_b32_e32 v180, 16, v193
	v_and_b32_e32 v181, 0xffff0000, v193
	v_rcp_f32_e32 v146, v146
	v_rcp_f32_e32 v147, v147
	v_exp_f32_e32 v128, v128
	v_exp_f32_e32 v129, v129
	v_mul_f32_e32 v130, 0xbfb8aa3b, v130
	v_mul_f32_e32 v131, 0xbfb8aa3b, v131
	v_pk_fma_f32 v[158:159], v[158:159], v[180:181], v[162:163]
	v_add_f32_e32 v140, 1.0, v140
	v_add_f32_e32 v141, 1.0, v141
	v_exp_f32_e32 v130, v130
	v_exp_f32_e32 v131, v131
	v_cvt_pk_bf16_f32 v156, v156, v157
	v_cvt_pk_bf16_f32 v157, v158, v159
	v_lshlrev_b32_e32 v158, 16, v198
	v_and_b32_e32 v159, 0xffff0000, v198
	v_lshlrev_b32_e32 v162, 16, v194
	v_and_b32_e32 v163, 0xffff0000, v194
	v_rcp_f32_e32 v140, v140
	v_rcp_f32_e32 v141, v141
	v_add_f32_e32 v142, 1.0, v142
	v_add_f32_e32 v143, 1.0, v143
	v_fma_f32 v116, v116, v250, v44
	v_fma_f32 v117, v117, v250, v45
	v_pk_fma_f32 v[144:145], v[144:145], v[162:163], v[158:159]
	v_lshlrev_b32_e32 v158, 16, v199
	v_and_b32_e32 v159, 0xffff0000, v199
	v_lshlrev_b32_e32 v162, 16, v195
	v_and_b32_e32 v163, 0xffff0000, v195
	v_rcp_f32_e32 v142, v142
	v_rcp_f32_e32 v143, v143
	v_mul_f32_e32 v116, 0xbfb8aa3b, v116
	v_mul_f32_e32 v117, 0xbfb8aa3b, v117
	v_fma_f32 v118, v118, v250, v46
	v_fma_f32 v119, v119, v250, v47
	v_pk_fma_f32 v[146:147], v[146:147], v[162:163], v[158:159]
	v_add_f32_e32 v128, 1.0, v128
	v_add_f32_e32 v129, 1.0, v129
	v_exp_f32_e32 v116, v116
	v_exp_f32_e32 v117, v117
	v_mul_f32_e32 v118, 0xbfb8aa3b, v118
	v_mul_f32_e32 v119, 0xbfb8aa3b, v119
	v_cvt_pk_bf16_f32 v158, v144, v145
	v_cvt_pk_bf16_f32 v159, v146, v147
	v_lshlrev_b32_e32 v144, 16, v184
	v_and_b32_e32 v145, 0xffff0000, v184
	v_lshlrev_b32_e32 v146, 16, v188
	v_and_b32_e32 v147, 0xffff0000, v188
	v_rcp_f32_e32 v128, v128
	v_rcp_f32_e32 v129, v129
	v_add_f32_e32 v130, 1.0, v130
	v_add_f32_e32 v131, 1.0, v131
	v_exp_f32_e32 v118, v118
	v_exp_f32_e32 v119, v119
	v_fma_f32 v112, v112, v250, v36
	v_fma_f32 v113, v113, v250, v37
	v_pk_fma_f32 v[140:141], v[140:141], v[146:147], v[144:145]
	v_lshlrev_b32_e32 v144, 16, v185
	v_and_b32_e32 v145, 0xffff0000, v185
	v_lshlrev_b32_e32 v146, 16, v189
	v_and_b32_e32 v147, 0xffff0000, v189
	v_rcp_f32_e32 v130, v130
	v_rcp_f32_e32 v131, v131
	v_mul_f32_e32 v112, 0xbfb8aa3b, v112
	v_mul_f32_e32 v113, 0xbfb8aa3b, v113
	v_fma_f32 v114, v114, v250, v38
	v_fma_f32 v115, v115, v250, v39
	v_pk_fma_f32 v[142:143], v[142:143], v[146:147], v[144:145]
	v_exp_f32_e32 v112, v112
	v_exp_f32_e32 v113, v113
	v_mul_f32_e32 v114, 0xbfb8aa3b, v114
	v_mul_f32_e32 v115, 0xbfb8aa3b, v115
	v_cvt_pk_bf16_f32 v140, v140, v141
	v_cvt_pk_bf16_f32 v141, v142, v143
	v_lshlrev_b32_e32 v142, 16, v186
	v_and_b32_e32 v143, 0xffff0000, v186
	v_lshlrev_b32_e32 v144, 16, v190
	v_and_b32_e32 v145, 0xffff0000, v190
	v_add_f32_e32 v116, 1.0, v116
	v_add_f32_e32 v117, 1.0, v117
	v_exp_f32_e32 v114, v114
	v_exp_f32_e32 v115, v115
	v_fma_f32 v108, v108, v249, v60
	v_fma_f32 v109, v109, v249, v61
	v_pk_fma_f32 v[128:129], v[128:129], v[144:145], v[142:143]
	v_lshlrev_b32_e32 v142, 16, v187
	v_and_b32_e32 v143, 0xffff0000, v187
	v_lshlrev_b32_e32 v144, 16, v191
	v_and_b32_e32 v145, 0xffff0000, v191
	v_rcp_f32_e32 v116, v116
	v_rcp_f32_e32 v117, v117
	v_add_f32_e32 v118, 1.0, v118
	v_add_f32_e32 v119, 1.0, v119
	v_mul_f32_e32 v108, 0xbfb8aa3b, v108
	v_mul_f32_e32 v109, 0xbfb8aa3b, v109
	v_fma_f32 v110, v110, v249, v62
	v_fma_f32 v111, v111, v249, v63
	v_pk_fma_f32 v[130:131], v[130:131], v[144:145], v[142:143]
	v_cvt_pk_bf16_f32 v142, v128, v129
	v_add_co_u32_e32 v128, vcc, s1, v160
	v_rcp_f32_e32 v118, v118
	v_rcp_f32_e32 v119, v119
	v_exp_f32_e32 v108, v108
	v_exp_f32_e32 v109, v109
	v_mul_f32_e32 v110, 0xbfb8aa3b, v110
	v_mul_f32_e32 v111, 0xbfb8aa3b, v111
	v_cvt_pk_bf16_f32 v143, v130, v131
	v_addc_co_u32_e32 v129, vcc, 0, v161, vcc
	v_add_f32_e32 v112, 1.0, v112
	v_add_f32_e32 v113, 1.0, v113
	v_exp_f32_e32 v110, v110
	v_exp_f32_e32 v111, v111
	v_fma_f32 v104, v104, v249, v52
	v_fma_f32 v105, v105, v249, v53
	global_store_dwordx4 v[128:129], v[140:143], off sc0 sc1
	v_lshlrev_b32_e32 v130, 16, v176
	v_and_b32_e32 v131, 0xffff0000, v176
	v_lshlrev_b32_e32 v140, 16, v172
	v_and_b32_e32 v141, 0xffff0000, v172
	v_rcp_f32_e32 v112, v112
	v_rcp_f32_e32 v113, v113
	v_add_f32_e32 v114, 1.0, v114
	v_add_f32_e32 v115, 1.0, v115
	v_mul_f32_e32 v104, 0xbfb8aa3b, v104
	v_mul_f32_e32 v105, 0xbfb8aa3b, v105
	v_fma_f32 v106, v106, v249, v54
	v_fma_f32 v107, v107, v249, v55
	v_pk_fma_f32 v[116:117], v[116:117], v[140:141], v[130:131]
	v_lshlrev_b32_e32 v130, 16, v177
	v_and_b32_e32 v131, 0xffff0000, v177
	v_lshlrev_b32_e32 v140, 16, v173
	v_and_b32_e32 v141, 0xffff0000, v173
	v_rcp_f32_e32 v114, v114
	v_rcp_f32_e32 v115, v115
	v_exp_f32_e32 v104, v104
	v_exp_f32_e32 v105, v105
	v_mul_f32_e32 v106, 0xbfb8aa3b, v106
	v_mul_f32_e32 v107, 0xbfb8aa3b, v107
	v_pk_fma_f32 v[118:119], v[118:119], v[140:141], v[130:131]
	v_add_f32_e32 v108, 1.0, v108
	v_add_f32_e32 v109, 1.0, v109
	v_exp_f32_e32 v106, v106
	v_exp_f32_e32 v107, v107
	v_cvt_pk_bf16_f32 v116, v116, v117
	v_cvt_pk_bf16_f32 v117, v118, v119
	v_lshlrev_b32_e32 v118, 16, v178
	v_and_b32_e32 v119, 0xffff0000, v178
	v_lshlrev_b32_e32 v130, 16, v174
	v_and_b32_e32 v131, 0xffff0000, v174
	v_rcp_f32_e32 v108, v108
	v_rcp_f32_e32 v109, v109
	v_add_f32_e32 v110, 1.0, v110
	v_add_f32_e32 v111, 1.0, v111
	v_fma_f32 v100, v100, v249, v44
	v_fma_f32 v101, v101, v249, v45
	v_pk_fma_f32 v[112:113], v[112:113], v[130:131], v[118:119]
	v_lshlrev_b32_e32 v118, 16, v179
	v_and_b32_e32 v119, 0xffff0000, v179
	v_lshlrev_b32_e32 v130, 16, v175
	v_and_b32_e32 v131, 0xffff0000, v175
	v_rcp_f32_e32 v110, v110
	v_rcp_f32_e32 v111, v111
	v_mul_f32_e32 v100, 0xbfb8aa3b, v100
	v_mul_f32_e32 v101, 0xbfb8aa3b, v101
	v_fma_f32 v102, v102, v249, v46
	v_fma_f32 v103, v103, v249, v47
	v_pk_fma_f32 v[114:115], v[114:115], v[130:131], v[118:119]
	v_add_f32_e32 v104, 1.0, v104
	v_add_f32_e32 v105, 1.0, v105
	v_exp_f32_e32 v100, v100
	v_exp_f32_e32 v101, v101
	v_mul_f32_e32 v102, 0xbfb8aa3b, v102
	v_mul_f32_e32 v103, 0xbfb8aa3b, v103
	v_cvt_pk_bf16_f32 v118, v112, v113
	v_cvt_pk_bf16_f32 v119, v114, v115
	v_lshlrev_b32_e32 v112, 16, v164
	v_and_b32_e32 v113, 0xffff0000, v164
	v_lshlrev_b32_e32 v114, 16, v168
	v_and_b32_e32 v115, 0xffff0000, v168
	v_rcp_f32_e32 v104, v104
	v_rcp_f32_e32 v105, v105
	v_add_f32_e32 v106, 1.0, v106
	v_add_f32_e32 v107, 1.0, v107
	v_exp_f32_e32 v102, v102
	v_exp_f32_e32 v103, v103
	v_fma_f32 v96, v96, v249, v36
	v_fma_f32 v97, v97, v249, v37
	v_pk_fma_f32 v[108:109], v[108:109], v[114:115], v[112:113]
	v_lshlrev_b32_e32 v112, 16, v165
	v_and_b32_e32 v113, 0xffff0000, v165
	v_lshlrev_b32_e32 v114, 16, v169
	v_and_b32_e32 v115, 0xffff0000, v169
	v_rcp_f32_e32 v106, v106
	v_rcp_f32_e32 v107, v107
	v_mul_f32_e32 v96, 0xbfb8aa3b, v96
	v_mul_f32_e32 v97, 0xbfb8aa3b, v97
	v_fma_f32 v98, v98, v249, v38
	v_fma_f32 v99, v99, v249, v39
	v_pk_fma_f32 v[110:111], v[110:111], v[114:115], v[112:113]
	v_exp_f32_e32 v96, v96
	v_exp_f32_e32 v97, v97
	v_mul_f32_e32 v98, 0xbfb8aa3b, v98
	v_mul_f32_e32 v99, 0xbfb8aa3b, v99
	v_cvt_pk_bf16_f32 v108, v108, v109
	v_cvt_pk_bf16_f32 v109, v110, v111
	v_lshlrev_b32_e32 v110, 16, v166
	v_and_b32_e32 v111, 0xffff0000, v166
	v_lshlrev_b32_e32 v112, 16, v170
	v_and_b32_e32 v113, 0xffff0000, v170
	v_add_f32_e32 v100, 1.0, v100
	v_add_f32_e32 v101, 1.0, v101
	v_exp_f32_e32 v98, v98
	v_exp_f32_e32 v99, v99
	v_fma_f32 v92, v92, v248, v60
	v_fma_f32 v93, v93, v248, v61
	v_pk_fma_f32 v[104:105], v[104:105], v[112:113], v[110:111]
	v_lshlrev_b32_e32 v110, 16, v167
	v_and_b32_e32 v111, 0xffff0000, v167
	v_lshlrev_b32_e32 v112, 16, v171
	v_and_b32_e32 v113, 0xffff0000, v171
	v_rcp_f32_e32 v100, v100
	v_rcp_f32_e32 v101, v101
	v_add_f32_e32 v102, 1.0, v102
	v_add_f32_e32 v103, 1.0, v103
	v_mul_f32_e32 v92, 0xbfb8aa3b, v92
	v_mul_f32_e32 v93, 0xbfb8aa3b, v93
	v_fma_f32 v94, v94, v248, v62
	v_fma_f32 v95, v95, v248, v63
	v_pk_fma_f32 v[106:107], v[106:107], v[112:113], v[110:111]
	v_cvt_pk_bf16_f32 v110, v104, v105
	v_add_co_u32_e32 v104, vcc, s52, v160
	v_rcp_f32_e32 v102, v102
	v_rcp_f32_e32 v103, v103
	v_exp_f32_e32 v92, v92
	v_exp_f32_e32 v93, v93
	v_mul_f32_e32 v94, 0xbfb8aa3b, v94
	v_mul_f32_e32 v95, 0xbfb8aa3b, v95
	v_cvt_pk_bf16_f32 v111, v106, v107
	v_addc_co_u32_e32 v105, vcc, 0, v161, vcc
	v_add_f32_e32 v96, 1.0, v96
	v_add_f32_e32 v97, 1.0, v97
	v_exp_f32_e32 v94, v94
	v_exp_f32_e32 v95, v95
	v_fma_f32 v88, v88, v248, v52
	v_fma_f32 v89, v89, v248, v53
	global_store_dwordx4 v[104:105], v[108:111], off sc0 sc1
	v_lshlrev_b32_e32 v106, 16, v152
	v_and_b32_e32 v107, 0xffff0000, v152
	v_lshlrev_b32_e32 v108, 16, v148
	v_and_b32_e32 v109, 0xffff0000, v148
	v_rcp_f32_e32 v96, v96
	v_rcp_f32_e32 v97, v97
	v_add_f32_e32 v98, 1.0, v98
	v_add_f32_e32 v99, 1.0, v99
	v_mul_f32_e32 v88, 0xbfb8aa3b, v88
	v_mul_f32_e32 v89, 0xbfb8aa3b, v89
	v_fma_f32 v90, v90, v248, v54
	v_fma_f32 v91, v91, v248, v55
	v_pk_fma_f32 v[100:101], v[100:101], v[108:109], v[106:107]
	v_lshlrev_b32_e32 v106, 16, v153
	v_and_b32_e32 v107, 0xffff0000, v153
	v_lshlrev_b32_e32 v108, 16, v149
	v_and_b32_e32 v109, 0xffff0000, v149
	v_rcp_f32_e32 v98, v98
	v_rcp_f32_e32 v99, v99
	v_exp_f32_e32 v88, v88
	v_exp_f32_e32 v89, v89
	v_mul_f32_e32 v90, 0xbfb8aa3b, v90
	v_mul_f32_e32 v91, 0xbfb8aa3b, v91
	v_pk_fma_f32 v[102:103], v[102:103], v[108:109], v[106:107]
	v_add_f32_e32 v92, 1.0, v92
	v_add_f32_e32 v93, 1.0, v93
	v_exp_f32_e32 v90, v90
	v_exp_f32_e32 v91, v91
	v_cvt_pk_bf16_f32 v100, v100, v101
	v_cvt_pk_bf16_f32 v101, v102, v103
	v_lshlrev_b32_e32 v102, 16, v154
	v_and_b32_e32 v103, 0xffff0000, v154
	v_lshlrev_b32_e32 v106, 16, v150
	v_and_b32_e32 v107, 0xffff0000, v150
	v_rcp_f32_e32 v92, v92
	v_rcp_f32_e32 v93, v93
	v_add_f32_e32 v94, 1.0, v94
	v_add_f32_e32 v95, 1.0, v95
	v_fma_f32 v84, v84, v248, v44
	v_fma_f32 v85, v85, v248, v45
	v_pk_fma_f32 v[96:97], v[96:97], v[106:107], v[102:103]
	v_lshlrev_b32_e32 v102, 16, v155
	v_and_b32_e32 v103, 0xffff0000, v155
	v_lshlrev_b32_e32 v106, 16, v151
	v_and_b32_e32 v107, 0xffff0000, v151
	v_rcp_f32_e32 v94, v94
	v_rcp_f32_e32 v95, v95
	v_mul_f32_e32 v84, 0xbfb8aa3b, v84
	v_mul_f32_e32 v85, 0xbfb8aa3b, v85
	v_fma_f32 v86, v86, v248, v46
	v_fma_f32 v87, v87, v248, v47
	v_pk_fma_f32 v[98:99], v[98:99], v[106:107], v[102:103]
	v_add_f32_e32 v88, 1.0, v88
	v_add_f32_e32 v89, 1.0, v89
	v_exp_f32_e32 v84, v84
	v_exp_f32_e32 v85, v85
	v_mul_f32_e32 v86, 0xbfb8aa3b, v86
	v_mul_f32_e32 v87, 0xbfb8aa3b, v87
	v_cvt_pk_bf16_f32 v102, v96, v97
	v_cvt_pk_bf16_f32 v103, v98, v99
	v_lshlrev_b32_e32 v96, 16, v132
	v_and_b32_e32 v97, 0xffff0000, v132
	s_waitcnt vmcnt(0)
	v_lshlrev_b32_e32 v98, 16, v136
	v_and_b32_e32 v99, 0xffff0000, v136
	v_rcp_f32_e32 v88, v88
	v_rcp_f32_e32 v89, v89
	v_add_f32_e32 v90, 1.0, v90
	v_add_f32_e32 v91, 1.0, v91
	v_exp_f32_e32 v86, v86
	v_exp_f32_e32 v87, v87
	v_fma_f32 v80, v80, v248, v36
	v_fma_f32 v81, v81, v248, v37
	v_pk_fma_f32 v[92:93], v[92:93], v[98:99], v[96:97]
	v_lshlrev_b32_e32 v96, 16, v133
	v_and_b32_e32 v97, 0xffff0000, v133
	v_lshlrev_b32_e32 v98, 16, v137
	v_and_b32_e32 v99, 0xffff0000, v137
	v_rcp_f32_e32 v90, v90
	v_rcp_f32_e32 v91, v91
	v_mul_f32_e32 v80, 0xbfb8aa3b, v80
	v_mul_f32_e32 v81, 0xbfb8aa3b, v81
	v_fma_f32 v82, v82, v248, v38
	v_fma_f32 v83, v83, v248, v39
	v_pk_fma_f32 v[94:95], v[94:95], v[98:99], v[96:97]
	v_exp_f32_e32 v80, v80
	v_exp_f32_e32 v81, v81
	v_mul_f32_e32 v82, 0xbfb8aa3b, v82
	v_mul_f32_e32 v83, 0xbfb8aa3b, v83
	v_cvt_pk_bf16_f32 v92, v92, v93
	v_cvt_pk_bf16_f32 v93, v94, v95
	v_lshlrev_b32_e32 v94, 16, v134
	v_and_b32_e32 v95, 0xffff0000, v134
	v_lshlrev_b32_e32 v96, 16, v138
	v_and_b32_e32 v97, 0xffff0000, v138
	v_add_f32_e32 v84, 1.0, v84
	v_add_f32_e32 v85, 1.0, v85
	v_exp_f32_e32 v82, v82
	v_exp_f32_e32 v83, v83
	v_pk_fma_f32 v[88:89], v[88:89], v[96:97], v[94:95]
	v_lshlrev_b32_e32 v94, 16, v135
	v_and_b32_e32 v95, 0xffff0000, v135
	v_lshlrev_b32_e32 v96, 16, v139
	v_and_b32_e32 v97, 0xffff0000, v139
	v_rcp_f32_e32 v84, v84
	v_rcp_f32_e32 v85, v85
	v_add_f32_e32 v86, 1.0, v86
	v_add_f32_e32 v87, 1.0, v87
	v_pk_fma_f32 v[90:91], v[90:91], v[96:97], v[94:95]
	v_cvt_pk_bf16_f32 v94, v88, v89
	v_add_co_u32_e32 v88, vcc, s53, v160
	v_rcp_f32_e32 v86, v86
	v_rcp_f32_e32 v87, v87
	v_cvt_pk_bf16_f32 v95, v90, v91
	v_addc_co_u32_e32 v89, vcc, 0, v161, vcc
	v_add_f32_e32 v80, 1.0, v80
	v_add_f32_e32 v81, 1.0, v81
	global_store_dwordx4 v[88:89], v[92:95], off sc0 sc1
	v_lshlrev_b32_e32 v90, 16, v120
	v_and_b32_e32 v91, 0xffff0000, v120
	v_lshlrev_b32_e32 v92, 16, v124
	v_and_b32_e32 v93, 0xffff0000, v124
	v_rcp_f32_e32 v80, v80
	v_rcp_f32_e32 v81, v81
	v_add_f32_e32 v82, 1.0, v82
	v_add_f32_e32 v83, 1.0, v83
	v_pk_fma_f32 v[84:85], v[84:85], v[92:93], v[90:91]
	v_lshlrev_b32_e32 v90, 16, v121
	v_and_b32_e32 v91, 0xffff0000, v121
	v_lshlrev_b32_e32 v92, 16, v125
	v_and_b32_e32 v93, 0xffff0000, v125
	v_rcp_f32_e32 v82, v82
	v_rcp_f32_e32 v83, v83
	v_pk_fma_f32 v[86:87], v[86:87], v[92:93], v[90:91]
	v_cvt_pk_bf16_f32 v84, v84, v85
	v_cvt_pk_bf16_f32 v85, v86, v87
	v_lshlrev_b32_e32 v86, 16, v122
	v_and_b32_e32 v87, 0xffff0000, v122
	v_lshlrev_b32_e32 v90, 16, v126
	v_and_b32_e32 v91, 0xffff0000, v126
	v_pk_fma_f32 v[80:81], v[80:81], v[90:91], v[86:87]
	v_lshlrev_b32_e32 v86, 16, v123
	v_and_b32_e32 v87, 0xffff0000, v123
	v_lshlrev_b32_e32 v90, 16, v127
	v_and_b32_e32 v91, 0xffff0000, v127
	v_pk_fma_f32 v[82:83], v[82:83], v[90:91], v[86:87]
	v_cvt_pk_bf16_f32 v86, v80, v81
	v_cvt_pk_bf16_f32 v87, v82, v83
	v_add_u32_e32 v80, s15, v245
	global_store_dwordx4 v[160:161], v[156:159], off offset:256 sc0 sc1
	global_store_dwordx4 v[128:129], v[116:119], off offset:256 sc0 sc1
	global_store_dwordx4 v[104:105], v[100:103], off offset:256 sc0 sc1
	global_store_dwordx4 v[88:89], v[84:87], off offset:256 sc0 sc1
	v_ashrrev_i32_e32 v81, 31, v80
	v_lshlrev_b64 v[82:83], 11, v[80:81]
	v_lshl_add_u64 v[80:81], v[80:81], 2, s[12:13]
	global_load_dword v149, v[80:81], off
	global_load_dword v148, v[80:81], off offset:64
	global_load_dword v147, v[80:81], off offset:128
	global_load_dword v146, v[80:81], off offset:192
	v_lshl_add_u64 v[80:81], v[82:83], 0, v[226:227]
	v_lshlrev_b64 v[144:145], 1, v[80:81]
	v_lshl_add_u64 v[80:81], s[4:5], 0, v[144:145]
	global_load_dwordx4 v[140:143], v[80:81], off
	v_lshl_add_u64 v[82:83], s[8:9], 0, v[144:145]
	global_load_dwordx4 v[136:139], v[82:83], off
	global_load_dwordx4 v[132:135], v[80:81], off offset:256
	global_load_dwordx4 v[128:131], v[82:83], off offset:256
	v_add_co_u32_e32 v84, vcc, s1, v80
	s_waitcnt vmcnt(0)
	v_fma_f32 v76, v76, v149, v60
	v_addc_co_u32_e32 v85, vcc, 0, v81, vcc
	global_load_dwordx4 v[120:123], v[84:85], off
	v_add_co_u32_e32 v86, vcc, s1, v82
	v_fma_f32 v77, v77, v149, v61
	s_nop 0
	v_addc_co_u32_e32 v87, vcc, 0, v83, vcc
	global_load_dwordx4 v[124:127], v[86:87], off
	global_load_dwordx4 v[112:115], v[84:85], off offset:256
	global_load_dwordx4 v[116:119], v[86:87], off offset:256
	v_add_co_u32_e32 v84, vcc, s52, v80
	v_fma_f32 v78, v78, v149, v62
	s_nop 0
	v_addc_co_u32_e32 v85, vcc, 0, v81, vcc
	global_load_dwordx4 v[104:107], v[84:85], off
	v_add_co_u32_e32 v86, vcc, s52, v82
	v_fma_f32 v79, v79, v149, v63
	s_nop 0
	v_addc_co_u32_e32 v87, vcc, 0, v83, vcc
	global_load_dwordx4 v[108:111], v[86:87], off
	global_load_dwordx4 v[96:99], v[84:85], off offset:256
	global_load_dwordx4 v[100:103], v[86:87], off offset:256
	v_add_co_u32_e32 v80, vcc, s53, v80
	v_mul_f32_e32 v76, 0xbfb8aa3b, v76
	s_nop 0
	v_addc_co_u32_e32 v81, vcc, 0, v81, vcc
	global_load_dwordx4 v[88:91], v[80:81], off
	v_add_co_u32_e32 v82, vcc, s53, v82
	v_mul_f32_e32 v77, 0xbfb8aa3b, v77
	s_nop 0
	v_addc_co_u32_e32 v83, vcc, 0, v83, vcc
	global_load_dwordx4 v[92:95], v[82:83], off
	global_load_dwordx4 v[84:87], v[80:81], off offset:256
	s_nop 0
	global_load_dwordx4 v[80:83], v[82:83], off offset:256
	v_mul_f32_e32 v78, 0xbfb8aa3b, v78
	v_mul_f32_e32 v79, 0xbfb8aa3b, v79
	v_exp_f32_e32 v76, v76
	v_exp_f32_e32 v77, v77
	v_exp_f32_e32 v78, v78
	v_exp_f32_e32 v79, v79
	v_fma_f32 v72, v72, v149, v52
	v_fma_f32 v73, v73, v149, v53
	v_mul_f32_e32 v72, 0xbfb8aa3b, v72
	v_mul_f32_e32 v73, 0xbfb8aa3b, v73
	v_fma_f32 v74, v74, v149, v54
	v_fma_f32 v75, v75, v149, v55
	v_exp_f32_e32 v72, v72
	v_exp_f32_e32 v73, v73
	v_mul_f32_e32 v74, 0xbfb8aa3b, v74
	v_mul_f32_e32 v75, 0xbfb8aa3b, v75
	v_exp_f32_e32 v74, v74
	v_exp_f32_e32 v75, v75
	v_add_f32_e32 v76, 1.0, v76
	v_add_f32_e32 v77, 1.0, v77
	v_add_f32_e32 v78, 1.0, v78
	v_add_f32_e32 v79, 1.0, v79
	v_fma_f32 v68, v68, v149, v44
	v_fma_f32 v69, v69, v149, v45
	v_rcp_f32_e32 v76, v76
	v_rcp_f32_e32 v77, v77
	v_rcp_f32_e32 v78, v78
	v_rcp_f32_e32 v79, v79
	v_mul_f32_e32 v68, 0xbfb8aa3b, v68
	v_mul_f32_e32 v69, 0xbfb8aa3b, v69
	v_fma_f32 v70, v70, v149, v46
	v_fma_f32 v71, v71, v149, v47
	v_add_f32_e32 v72, 1.0, v72
	v_add_f32_e32 v73, 1.0, v73
	v_exp_f32_e32 v68, v68
	v_exp_f32_e32 v69, v69
	v_mul_f32_e32 v70, 0xbfb8aa3b, v70
	v_mul_f32_e32 v71, 0xbfb8aa3b, v71
	v_rcp_f32_e32 v72, v72
	v_rcp_f32_e32 v73, v73
	v_add_f32_e32 v74, 1.0, v74
	v_add_f32_e32 v75, 1.0, v75
	v_exp_f32_e32 v70, v70
	v_exp_f32_e32 v71, v71
	v_fma_f32 v64, v64, v149, v36
	v_fma_f32 v65, v65, v149, v37
	v_lshlrev_b32_e32 v150, 16, v140
	v_and_b32_e32 v151, 0xffff0000, v140
	v_lshlrev_b32_e32 v152, 16, v136
	v_and_b32_e32 v153, 0xffff0000, v136
	v_lshlrev_b32_e32 v140, 16, v141
	v_and_b32_e32 v141, 0xffff0000, v141
	v_lshlrev_b32_e32 v136, 16, v137
	v_and_b32_e32 v137, 0xffff0000, v137
	v_rcp_f32_e32 v74, v74
	v_rcp_f32_e32 v75, v75
	v_mul_f32_e32 v64, 0xbfb8aa3b, v64
	v_mul_f32_e32 v65, 0xbfb8aa3b, v65
	v_fma_f32 v66, v66, v149, v38
	v_fma_f32 v67, v67, v149, v39
	v_pk_fma_f32 v[76:77], v[76:77], v[152:153], v[150:151]
	v_pk_fma_f32 v[78:79], v[78:79], v[136:137], v[140:141]
	v_exp_f32_e32 v64, v64
	v_exp_f32_e32 v65, v65
	v_mul_f32_e32 v66, 0xbfb8aa3b, v66
	v_mul_f32_e32 v67, 0xbfb8aa3b, v67
	v_cvt_pk_bf16_f32 v76, v76, v77
	v_cvt_pk_bf16_f32 v77, v78, v79
	v_lshlrev_b32_e32 v78, 16, v142
	v_and_b32_e32 v79, 0xffff0000, v142
	v_lshlrev_b32_e32 v136, 16, v138
	v_and_b32_e32 v137, 0xffff0000, v138
	v_add_f32_e32 v68, 1.0, v68
	v_add_f32_e32 v69, 1.0, v69
	v_exp_f32_e32 v66, v66
	v_exp_f32_e32 v67, v67
	v_fma_f32 v56, v56, v148, v60
	v_fma_f32 v57, v57, v148, v61
	v_pk_fma_f32 v[72:73], v[72:73], v[136:137], v[78:79]
	v_lshlrev_b32_e32 v78, 16, v143
	v_and_b32_e32 v79, 0xffff0000, v143
	v_lshlrev_b32_e32 v136, 16, v139
	v_and_b32_e32 v137, 0xffff0000, v139
	v_rcp_f32_e32 v68, v68
	v_rcp_f32_e32 v69, v69
	v_add_f32_e32 v70, 1.0, v70
	v_add_f32_e32 v71, 1.0, v71
	v_mul_f32_e32 v56, 0xbfb8aa3b, v56
	v_mul_f32_e32 v57, 0xbfb8aa3b, v57
	v_fma_f32 v58, v58, v148, v62
	v_fma_f32 v59, v59, v148, v63
	v_pk_fma_f32 v[74:75], v[74:75], v[136:137], v[78:79]
	v_rcp_f32_e32 v70, v70
	v_rcp_f32_e32 v71, v71
	v_exp_f32_e32 v56, v56
	v_exp_f32_e32 v57, v57
	v_mul_f32_e32 v58, 0xbfb8aa3b, v58
	v_mul_f32_e32 v59, 0xbfb8aa3b, v59
	v_cvt_pk_bf16_f32 v78, v72, v73
	v_cvt_pk_bf16_f32 v79, v74, v75
	v_lshl_add_u64 v[72:73], s[6:7], 0, v[144:145]
	v_add_f32_e32 v64, 1.0, v64
	v_add_f32_e32 v65, 1.0, v65
	v_exp_f32_e32 v58, v58
	v_exp_f32_e32 v59, v59
	v_fma_f32 v48, v48, v148, v52
	v_fma_f32 v49, v49, v148, v53
	global_store_dwordx4 v[72:73], v[76:79], off sc0 sc1
	v_lshlrev_b32_e32 v74, 16, v132
	v_and_b32_e32 v75, 0xffff0000, v132
	v_lshlrev_b32_e32 v76, 16, v128
	v_and_b32_e32 v77, 0xffff0000, v128
	v_rcp_f32_e32 v64, v64
	v_rcp_f32_e32 v65, v65
	v_add_f32_e32 v66, 1.0, v66
	v_add_f32_e32 v67, 1.0, v67
	v_mul_f32_e32 v48, 0xbfb8aa3b, v48
	v_mul_f32_e32 v49, 0xbfb8aa3b, v49
	v_fma_f32 v50, v50, v148, v54
	v_fma_f32 v51, v51, v148, v55
	v_pk_fma_f32 v[68:69], v[68:69], v[76:77], v[74:75]
	v_lshlrev_b32_e32 v74, 16, v133
	v_and_b32_e32 v75, 0xffff0000, v133
	v_lshlrev_b32_e32 v76, 16, v129
	v_and_b32_e32 v77, 0xffff0000, v129
	v_rcp_f32_e32 v66, v66
	v_rcp_f32_e32 v67, v67
	v_exp_f32_e32 v48, v48
	v_exp_f32_e32 v49, v49
	v_mul_f32_e32 v50, 0xbfb8aa3b, v50
	v_mul_f32_e32 v51, 0xbfb8aa3b, v51
	v_pk_fma_f32 v[70:71], v[70:71], v[76:77], v[74:75]
	v_add_f32_e32 v56, 1.0, v56
	v_add_f32_e32 v57, 1.0, v57
	v_exp_f32_e32 v50, v50
	v_exp_f32_e32 v51, v51
	v_cvt_pk_bf16_f32 v68, v68, v69
	v_cvt_pk_bf16_f32 v69, v70, v71
	v_lshlrev_b32_e32 v70, 16, v134
	v_and_b32_e32 v71, 0xffff0000, v134
	v_lshlrev_b32_e32 v74, 16, v130
	v_and_b32_e32 v75, 0xffff0000, v130
	v_rcp_f32_e32 v56, v56
	v_rcp_f32_e32 v57, v57
	v_add_f32_e32 v58, 1.0, v58
	v_add_f32_e32 v59, 1.0, v59
	v_fma_f32 v40, v40, v148, v44
	v_fma_f32 v41, v41, v148, v45
	v_pk_fma_f32 v[64:65], v[64:65], v[74:75], v[70:71]
	v_lshlrev_b32_e32 v70, 16, v135
	v_and_b32_e32 v71, 0xffff0000, v135
	v_lshlrev_b32_e32 v74, 16, v131
	v_and_b32_e32 v75, 0xffff0000, v131
	v_rcp_f32_e32 v58, v58
	v_rcp_f32_e32 v59, v59
	v_mul_f32_e32 v40, 0xbfb8aa3b, v40
	v_mul_f32_e32 v41, 0xbfb8aa3b, v41
	v_fma_f32 v42, v42, v148, v46
	v_fma_f32 v43, v43, v148, v47
	v_pk_fma_f32 v[66:67], v[66:67], v[74:75], v[70:71]
	v_add_f32_e32 v48, 1.0, v48
	v_add_f32_e32 v49, 1.0, v49
	v_exp_f32_e32 v40, v40
	v_exp_f32_e32 v41, v41
	v_mul_f32_e32 v42, 0xbfb8aa3b, v42
	v_mul_f32_e32 v43, 0xbfb8aa3b, v43
	v_cvt_pk_bf16_f32 v70, v64, v65
	v_cvt_pk_bf16_f32 v71, v66, v67
	s_waitcnt vmcnt(0)
	v_lshlrev_b32_e32 v64, 16, v120
	v_and_b32_e32 v65, 0xffff0000, v120
	v_lshlrev_b32_e32 v66, 16, v124
	v_and_b32_e32 v67, 0xffff0000, v124
	v_rcp_f32_e32 v48, v48
	v_rcp_f32_e32 v49, v49
	v_add_f32_e32 v50, 1.0, v50
	v_add_f32_e32 v51, 1.0, v51
	v_exp_f32_e32 v42, v42
	v_exp_f32_e32 v43, v43
	v_fma_f32 v32, v32, v148, v36
	v_fma_f32 v33, v33, v148, v37
	v_pk_fma_f32 v[56:57], v[56:57], v[66:67], v[64:65]
	v_lshlrev_b32_e32 v64, 16, v121
	v_and_b32_e32 v65, 0xffff0000, v121
	v_lshlrev_b32_e32 v66, 16, v125
	v_and_b32_e32 v67, 0xffff0000, v125
	v_rcp_f32_e32 v50, v50
	v_rcp_f32_e32 v51, v51
	v_mul_f32_e32 v32, 0xbfb8aa3b, v32
	v_mul_f32_e32 v33, 0xbfb8aa3b, v33
	v_fma_f32 v34, v34, v148, v38
	v_fma_f32 v35, v35, v148, v39
	v_pk_fma_f32 v[58:59], v[58:59], v[66:67], v[64:65]
	v_exp_f32_e32 v32, v32
	v_exp_f32_e32 v33, v33
	v_mul_f32_e32 v34, 0xbfb8aa3b, v34
	v_mul_f32_e32 v35, 0xbfb8aa3b, v35
	v_cvt_pk_bf16_f32 v56, v56, v57
	v_cvt_pk_bf16_f32 v57, v58, v59
	v_lshlrev_b32_e32 v58, 16, v122
	v_and_b32_e32 v59, 0xffff0000, v122
	v_lshlrev_b32_e32 v64, 16, v126
	v_and_b32_e32 v65, 0xffff0000, v126
	v_add_f32_e32 v40, 1.0, v40
	v_add_f32_e32 v41, 1.0, v41
	v_exp_f32_e32 v34, v34
	v_exp_f32_e32 v35, v35
	v_fma_f32 v28, v28, v147, v60
	v_fma_f32 v29, v29, v147, v61
	v_pk_fma_f32 v[48:49], v[48:49], v[64:65], v[58:59]
	v_lshlrev_b32_e32 v58, 16, v123
	v_and_b32_e32 v59, 0xffff0000, v123
	v_lshlrev_b32_e32 v64, 16, v127
	v_and_b32_e32 v65, 0xffff0000, v127
	v_rcp_f32_e32 v40, v40
	v_rcp_f32_e32 v41, v41
	v_add_f32_e32 v42, 1.0, v42
	v_add_f32_e32 v43, 1.0, v43
	v_mul_f32_e32 v28, 0xbfb8aa3b, v28
	v_mul_f32_e32 v29, 0xbfb8aa3b, v29
	v_fma_f32 v30, v30, v147, v62
	v_fma_f32 v31, v31, v147, v63
	v_pk_fma_f32 v[50:51], v[50:51], v[64:65], v[58:59]
	v_cvt_pk_bf16_f32 v58, v48, v49
	v_add_co_u32_e32 v48, vcc, s1, v72
	v_rcp_f32_e32 v42, v42
	v_rcp_f32_e32 v43, v43
	v_exp_f32_e32 v28, v28
	v_exp_f32_e32 v29, v29
	v_mul_f32_e32 v30, 0xbfb8aa3b, v30
	v_mul_f32_e32 v31, 0xbfb8aa3b, v31
	v_cvt_pk_bf16_f32 v59, v50, v51
	v_addc_co_u32_e32 v49, vcc, 0, v73, vcc
	v_add_f32_e32 v32, 1.0, v32
	v_add_f32_e32 v33, 1.0, v33
	v_exp_f32_e32 v30, v30
	v_exp_f32_e32 v31, v31
	v_fma_f32 v24, v24, v147, v52
	v_fma_f32 v25, v25, v147, v53
	global_store_dwordx4 v[48:49], v[56:59], off sc0 sc1
	v_lshlrev_b32_e32 v50, 16, v112
	v_and_b32_e32 v51, 0xffff0000, v112
	v_lshlrev_b32_e32 v56, 16, v116
	v_and_b32_e32 v57, 0xffff0000, v116
	v_rcp_f32_e32 v32, v32
	v_rcp_f32_e32 v33, v33
	v_add_f32_e32 v34, 1.0, v34
	v_add_f32_e32 v35, 1.0, v35
	v_mul_f32_e32 v24, 0xbfb8aa3b, v24
	v_mul_f32_e32 v25, 0xbfb8aa3b, v25
	v_fma_f32 v26, v26, v147, v54
	v_fma_f32 v27, v27, v147, v55
	v_pk_fma_f32 v[40:41], v[40:41], v[56:57], v[50:51]
	v_lshlrev_b32_e32 v50, 16, v113
	v_and_b32_e32 v51, 0xffff0000, v113
	v_lshlrev_b32_e32 v56, 16, v117
	v_and_b32_e32 v57, 0xffff0000, v117
	v_rcp_f32_e32 v34, v34
	v_rcp_f32_e32 v35, v35
	v_exp_f32_e32 v24, v24
	v_exp_f32_e32 v25, v25
	v_mul_f32_e32 v26, 0xbfb8aa3b, v26
	v_mul_f32_e32 v27, 0xbfb8aa3b, v27
	v_pk_fma_f32 v[42:43], v[42:43], v[56:57], v[50:51]
	v_add_f32_e32 v28, 1.0, v28
	v_add_f32_e32 v29, 1.0, v29
	v_exp_f32_e32 v26, v26
	v_exp_f32_e32 v27, v27
	v_cvt_pk_bf16_f32 v40, v40, v41
	v_cvt_pk_bf16_f32 v41, v42, v43
	v_lshlrev_b32_e32 v42, 16, v114
	v_and_b32_e32 v43, 0xffff0000, v114
	v_lshlrev_b32_e32 v50, 16, v118
	v_and_b32_e32 v51, 0xffff0000, v118
	v_rcp_f32_e32 v28, v28
	v_rcp_f32_e32 v29, v29
	v_add_f32_e32 v30, 1.0, v30
	v_add_f32_e32 v31, 1.0, v31
	v_fma_f32 v20, v20, v147, v44
	v_fma_f32 v21, v21, v147, v45
	v_pk_fma_f32 v[32:33], v[32:33], v[50:51], v[42:43]
	v_lshlrev_b32_e32 v42, 16, v115
	v_and_b32_e32 v43, 0xffff0000, v115
	v_lshlrev_b32_e32 v50, 16, v119
	v_and_b32_e32 v51, 0xffff0000, v119
	v_rcp_f32_e32 v30, v30
	v_rcp_f32_e32 v31, v31
	v_mul_f32_e32 v20, 0xbfb8aa3b, v20
	v_mul_f32_e32 v21, 0xbfb8aa3b, v21
	v_fma_f32 v22, v22, v147, v46
	v_fma_f32 v23, v23, v147, v47
	v_pk_fma_f32 v[34:35], v[34:35], v[50:51], v[42:43]
	v_add_f32_e32 v24, 1.0, v24
	v_add_f32_e32 v25, 1.0, v25
	v_exp_f32_e32 v20, v20
	v_exp_f32_e32 v21, v21
	v_mul_f32_e32 v22, 0xbfb8aa3b, v22
	v_mul_f32_e32 v23, 0xbfb8aa3b, v23
	v_cvt_pk_bf16_f32 v42, v32, v33
	v_cvt_pk_bf16_f32 v43, v34, v35
	v_lshlrev_b32_e32 v32, 16, v104
	v_and_b32_e32 v33, 0xffff0000, v104
	v_lshlrev_b32_e32 v34, 16, v108
	v_and_b32_e32 v35, 0xffff0000, v108
	v_rcp_f32_e32 v24, v24
	v_rcp_f32_e32 v25, v25
	v_add_f32_e32 v26, 1.0, v26
	v_add_f32_e32 v27, 1.0, v27
	v_exp_f32_e32 v22, v22
	v_exp_f32_e32 v23, v23
	v_fma_f32 v16, v16, v147, v36
	v_fma_f32 v17, v17, v147, v37
	v_pk_fma_f32 v[28:29], v[28:29], v[34:35], v[32:33]
	v_lshlrev_b32_e32 v32, 16, v105
	v_and_b32_e32 v33, 0xffff0000, v105
	v_lshlrev_b32_e32 v34, 16, v109
	v_and_b32_e32 v35, 0xffff0000, v109
	v_rcp_f32_e32 v26, v26
	v_rcp_f32_e32 v27, v27
	v_mul_f32_e32 v16, 0xbfb8aa3b, v16
	v_mul_f32_e32 v17, 0xbfb8aa3b, v17
	v_fma_f32 v18, v18, v147, v38
	v_fma_f32 v19, v19, v147, v39
	v_pk_fma_f32 v[30:31], v[30:31], v[34:35], v[32:33]
	v_exp_f32_e32 v16, v16
	v_exp_f32_e32 v17, v17
	v_mul_f32_e32 v18, 0xbfb8aa3b, v18
	v_mul_f32_e32 v19, 0xbfb8aa3b, v19
	v_cvt_pk_bf16_f32 v28, v28, v29
	v_cvt_pk_bf16_f32 v29, v30, v31
	v_lshlrev_b32_e32 v30, 16, v106
	v_and_b32_e32 v31, 0xffff0000, v106
	v_lshlrev_b32_e32 v32, 16, v110
	v_and_b32_e32 v33, 0xffff0000, v110
	v_add_f32_e32 v20, 1.0, v20
	v_add_f32_e32 v21, 1.0, v21
	v_exp_f32_e32 v18, v18
	v_exp_f32_e32 v19, v19
	v_fma_f32 v12, v12, v146, v60
	v_fma_f32 v13, v13, v146, v61
	v_pk_fma_f32 v[24:25], v[24:25], v[32:33], v[30:31]
	v_lshlrev_b32_e32 v30, 16, v107
	v_and_b32_e32 v31, 0xffff0000, v107
	v_lshlrev_b32_e32 v32, 16, v111
	v_and_b32_e32 v33, 0xffff0000, v111
	v_rcp_f32_e32 v20, v20
	v_rcp_f32_e32 v21, v21
	v_add_f32_e32 v22, 1.0, v22
	v_add_f32_e32 v23, 1.0, v23
	v_mul_f32_e32 v12, 0xbfb8aa3b, v12
	v_mul_f32_e32 v13, 0xbfb8aa3b, v13
	v_fma_f32 v14, v14, v146, v62
	v_fmac_f32_e32 v63, v15, v146
	v_pk_fma_f32 v[26:27], v[26:27], v[32:33], v[30:31]
	v_cvt_pk_bf16_f32 v30, v24, v25
	v_add_co_u32_e32 v24, vcc, s52, v72
	v_rcp_f32_e32 v22, v22
	v_rcp_f32_e32 v23, v23
	v_exp_f32_e32 v12, v12
	v_exp_f32_e32 v13, v13
	v_mul_f32_e32 v14, 0xbfb8aa3b, v14
	v_mul_f32_e32 v15, 0xbfb8aa3b, v63
	v_cvt_pk_bf16_f32 v31, v26, v27
	v_addc_co_u32_e32 v25, vcc, 0, v73, vcc
	v_add_f32_e32 v16, 1.0, v16
	v_add_f32_e32 v17, 1.0, v17
	v_exp_f32_e32 v14, v14
	v_exp_f32_e32 v15, v15
	v_fma_f32 v8, v8, v146, v52
	v_fma_f32 v9, v9, v146, v53
	global_store_dwordx4 v[24:25], v[28:31], off sc0 sc1
	v_lshlrev_b32_e32 v26, 16, v96
	v_and_b32_e32 v27, 0xffff0000, v96
	v_lshlrev_b32_e32 v28, 16, v100
	v_and_b32_e32 v29, 0xffff0000, v100
	v_rcp_f32_e32 v16, v16
	v_rcp_f32_e32 v17, v17
	v_add_f32_e32 v18, 1.0, v18
	v_add_f32_e32 v19, 1.0, v19
	v_mul_f32_e32 v8, 0xbfb8aa3b, v8
	v_mul_f32_e32 v9, 0xbfb8aa3b, v9
	v_fma_f32 v10, v10, v146, v54
	v_fmac_f32_e32 v55, v11, v146
	v_pk_fma_f32 v[20:21], v[20:21], v[28:29], v[26:27]
	v_lshlrev_b32_e32 v26, 16, v97
	v_and_b32_e32 v27, 0xffff0000, v97
	v_lshlrev_b32_e32 v28, 16, v101
	v_and_b32_e32 v29, 0xffff0000, v101
	v_rcp_f32_e32 v18, v18
	v_rcp_f32_e32 v19, v19
	v_exp_f32_e32 v8, v8
	v_exp_f32_e32 v9, v9
	v_mul_f32_e32 v10, 0xbfb8aa3b, v10
	v_mul_f32_e32 v11, 0xbfb8aa3b, v55
	v_pk_fma_f32 v[22:23], v[22:23], v[28:29], v[26:27]
	v_add_f32_e32 v12, 1.0, v12
	v_add_f32_e32 v13, 1.0, v13
	v_exp_f32_e32 v10, v10
	v_exp_f32_e32 v11, v11
	v_cvt_pk_bf16_f32 v20, v20, v21
	v_cvt_pk_bf16_f32 v21, v22, v23
	v_lshlrev_b32_e32 v22, 16, v98
	v_and_b32_e32 v23, 0xffff0000, v98
	v_lshlrev_b32_e32 v26, 16, v102
	v_and_b32_e32 v27, 0xffff0000, v102
	v_rcp_f32_e32 v12, v12
	v_rcp_f32_e32 v13, v13
	v_add_f32_e32 v14, 1.0, v14
	v_add_f32_e32 v15, 1.0, v15
	v_fma_f32 v4, v4, v146, v44
	v_fma_f32 v5, v5, v146, v45
	v_pk_fma_f32 v[16:17], v[16:17], v[26:27], v[22:23]
	v_lshlrev_b32_e32 v22, 16, v99
	v_and_b32_e32 v23, 0xffff0000, v99
	v_lshlrev_b32_e32 v26, 16, v103
	v_and_b32_e32 v27, 0xffff0000, v103
	v_rcp_f32_e32 v14, v14
	v_rcp_f32_e32 v15, v15
	v_mul_f32_e32 v4, 0xbfb8aa3b, v4
	v_mul_f32_e32 v5, 0xbfb8aa3b, v5
	v_pk_fma_f32 v[18:19], v[18:19], v[26:27], v[22:23]
	v_add_f32_e32 v8, 1.0, v8
	v_add_f32_e32 v9, 1.0, v9
	v_exp_f32_e32 v4, v4
	v_exp_f32_e32 v5, v5
	v_cvt_pk_bf16_f32 v22, v16, v17
	v_cvt_pk_bf16_f32 v23, v18, v19
	v_lshlrev_b32_e32 v16, 16, v88
	v_and_b32_e32 v17, 0xffff0000, v88
	v_lshlrev_b32_e32 v18, 16, v92
	v_and_b32_e32 v19, 0xffff0000, v92
	v_rcp_f32_e32 v8, v8
	v_rcp_f32_e32 v9, v9
	v_add_f32_e32 v10, 1.0, v10
	v_add_f32_e32 v11, 1.0, v11
	v_pk_fma_f32 v[12:13], v[12:13], v[18:19], v[16:17]
	v_lshlrev_b32_e32 v16, 16, v89
	v_and_b32_e32 v17, 0xffff0000, v89
	v_lshlrev_b32_e32 v18, 16, v93
	v_and_b32_e32 v19, 0xffff0000, v93
	v_rcp_f32_e32 v10, v10
	v_rcp_f32_e32 v11, v11
	v_pk_fma_f32 v[14:15], v[14:15], v[18:19], v[16:17]
	v_cvt_pk_bf16_f32 v12, v12, v13
	v_cvt_pk_bf16_f32 v13, v14, v15
	v_lshlrev_b32_e32 v14, 16, v90
	v_and_b32_e32 v15, 0xffff0000, v90
	v_lshlrev_b32_e32 v16, 16, v94
	v_and_b32_e32 v17, 0xffff0000, v94
	v_add_f32_e32 v4, 1.0, v4
	v_add_f32_e32 v5, 1.0, v5
	v_pk_fma_f32 v[8:9], v[8:9], v[16:17], v[14:15]
	v_lshlrev_b32_e32 v14, 16, v91
	v_and_b32_e32 v15, 0xffff0000, v91
	v_lshlrev_b32_e32 v16, 16, v95
	v_and_b32_e32 v17, 0xffff0000, v95
	v_rcp_f32_e32 v4, v4
	v_rcp_f32_e32 v5, v5
	v_pk_fma_f32 v[10:11], v[10:11], v[16:17], v[14:15]
	v_cvt_pk_bf16_f32 v14, v8, v9
	v_add_co_u32_e32 v8, vcc, s53, v72
	v_cvt_pk_bf16_f32 v15, v10, v11
	s_nop 0
	v_addc_co_u32_e32 v9, vcc, 0, v73, vcc
	global_store_dwordx4 v[8:9], v[12:15], off sc0 sc1
	v_lshlrev_b32_e32 v10, 16, v80
	v_and_b32_e32 v11, 0xffff0000, v80
	v_lshlrev_b32_e32 v12, 16, v84
	v_and_b32_e32 v13, 0xffff0000, v84
	v_pk_fma_f32 v[4:5], v[4:5], v[10:11], v[12:13]
	v_fmac_f32_e32 v47, v7, v146
	v_cvt_pk_bf16_f32 v4, v4, v5
	v_fma_f32 v5, v6, v146, v46
	v_mul_f32_e32 v5, 0xbfb8aa3b, v5
	v_exp_f32_e32 v5, v5
	v_fma_f32 v0, v0, v146, v36
	v_fma_f32 v1, v1, v146, v37
	v_mul_f32_e32 v0, 0xbfb8aa3b, v0
	v_add_f32_e32 v5, 1.0, v5
	v_rcp_f32_e32 v6, v5
	v_mul_f32_e32 v5, 0xbfb8aa3b, v47
	v_exp_f32_e32 v5, v5
	v_mul_f32_e32 v1, 0xbfb8aa3b, v1
	v_fma_f32 v2, v2, v146, v38
	v_fmac_f32_e32 v39, v3, v146
	v_exp_f32_e32 v0, v0
	v_exp_f32_e32 v1, v1
	v_mul_f32_e32 v2, 0xbfb8aa3b, v2
	v_mul_f32_e32 v3, 0xbfb8aa3b, v39
	v_exp_f32_e32 v2, v2
	v_exp_f32_e32 v3, v3
	v_add_f32_e32 v5, 1.0, v5
	v_rcp_f32_e32 v7, v5
	v_add_f32_e32 v0, 1.0, v0
	v_add_f32_e32 v1, 1.0, v1
	v_rcp_f32_e32 v0, v0
	v_rcp_f32_e32 v1, v1
	v_add_f32_e32 v2, 1.0, v2
	v_add_f32_e32 v3, 1.0, v3
	v_lshlrev_b32_e32 v10, 16, v81
	v_and_b32_e32 v11, 0xffff0000, v81
	v_lshlrev_b32_e32 v12, 16, v85
	v_and_b32_e32 v13, 0xffff0000, v85
	v_rcp_f32_e32 v2, v2
	v_rcp_f32_e32 v3, v3
	v_pk_fma_f32 v[6:7], v[6:7], v[10:11], v[12:13]
	v_lshlrev_b32_e32 v10, 16, v82
	v_cvt_pk_bf16_f32 v5, v6, v7
	v_lshlrev_b32_e32 v6, 16, v86
	v_and_b32_e32 v7, 0xffff0000, v86
	v_and_b32_e32 v11, 0xffff0000, v82
	v_pk_fma_f32 v[0:1], v[0:1], v[10:11], v[6:7]
	v_lshlrev_b32_e32 v6, 16, v87
	v_and_b32_e32 v7, 0xffff0000, v87
	v_lshlrev_b32_e32 v10, 16, v83
	v_and_b32_e32 v11, 0xffff0000, v83
	v_pk_fma_f32 v[2:3], v[2:3], v[10:11], v[6:7]
	v_cvt_pk_bf16_f32 v6, v0, v1
	v_cvt_pk_bf16_f32 v7, v2, v3
	global_store_dwordx4 v[72:73], v[68:71], off offset:256 sc0 sc1
	global_store_dwordx4 v[48:49], v[40:43], off offset:256 sc0 sc1
	global_store_dwordx4 v[24:25], v[20:23], off offset:256 sc0 sc1
	global_store_dwordx4 v[8:9], v[4:7], off offset:256 sc0 sc1
	s_and_b64 vcc, exec, s[2:3]
	s_cbranch_vccz .LBB0_1438
	s_waitcnt vmcnt(0)
	s_cmpk_gt_u32 s56, 0xff
	s_cbranch_scc1 .LBB0_1449
	s_barrier
